# O2: next head's v-row loads stay in flight across the MFMA stage (counted vmcnt(8) instead of vmcnt(0) on that path)
# baseline (speedup 1.0000x reference)
; #define LAS __attribute__((address_space(3)))
; __device__ __forceinline__ void phase_sgu(CArgs a, LAS unsigned char* lds, int i2, int wv, int xw  ) {
;     ...
;             asm volatile("s_waitcnt vmcnt(0)" ::: "memory");
;             __syncthreads();
;             u32x2 uvp[4][4]; float bsp[4];
; #pragma unroll
;             for (int m = 0; m < 4; ++m) bsp[m] = a->in[I_SGUB][((size_t)i2 * 8 + h) * 128 + wr * 64 + m * 16 + fr];
; #pragma unroll
;             for (int m = 0; m < 4; ++m)
; #pragma unroll
;                 for (int n = 0; n < 4; ++n) uvp[m][n] = *(const u32x2*)(HB + (tok0 + wr * 64 + m * 16 + fr) * (2 * SGU_W) + h * 256 + wc * 64 + n * 16 + 4 * fq);
;             f32x4 acc[4][4];
; #pragma unroll
;             for (int m = 0; m < 4; ++m)
; #pragma unroll
;                 for (int n = 0; n < 4; ++n) acc[m][n] = (f32x4){0.f, 0.f, 0.f, 0.f};
; #pragma unroll
;             for (int ks = 0; ks < 4; ++ks) {
;                 bf16x8 bfr[4], af[4];
; #pragma unroll
;                 for (int m = 0; m < 4; ++m) { const int i = wr * 64 + m * 16 + fr; af[m] = *(const LAS bf16x8*)(wl + i * 256 + (((ks * 4 + fq) ^ (i & 15)) * 16)); }
; #pragma unroll
;                 for (int n = 0; n < 4; ++n) bfr[n] = *(const LAS bf16x8*)(vt + (wc * 64 + n * 16 + fr) * VS + ks * 32 + fq * 8);
; #pragma unroll
;                 for (int m = 0; m < 4; ++m)
; #pragma unroll
;                     for (int n = 0; n < 4; ++n) acc[m][n] = __builtin_amdgcn_mfma_f32_16x16x32_bf16(bfr[n], af[m], acc[m][n], 0, 0, 0);
.Lo2_rows_inflight:
	s_waitcnt lgkmcnt(0)
	s_barrier
	s_load_dwordx2 s[22:23], s[2:3], 0x88
	s_add_u32 s6, s6, 0x400
	s_addc_u32 s7, s7, 0
	v_lshl_add_u64 v[116:117], v[116:117], 0, s[60:61]
	v_lshl_add_u64 v[122:123], v[122:123], 0, s[60:61]
	s_waitcnt lgkmcnt(0)
	v_lshl_add_u64 v[32:33], s[22:23], 0, v[132:133]
	global_load_dword v168, v[32:33], off
	global_load_dword v156, v[32:33], off offset:64
	global_load_dword v144, v[32:33], off offset:128
	global_load_dword v134, v[32:33], off offset:192
	v_lshl_add_u64 v[32:33], s[4:5], 0, v[120:121]
	v_add_co_u32_e32 v34, vcc, s71, v32
	s_mov_b32 s22, 0x3a020000
	s_nop 0
	v_addc_co_u32_e32 v35, vcc, 0, v33, vcc
	global_load_dwordx2 v[174:175], v[34:35], off
	global_load_dwordx2 v[172:173], v[34:35], off offset:32
	global_load_dwordx2 v[170:171], v[34:35], off offset:64
	global_load_dwordx2 v[166:167], v[34:35], off offset:96
	v_add_co_u32_e32 v34, vcc, s22, v32
	s_mov_b32 s22, 0x3a040000
	s_nop 0
	v_addc_co_u32_e32 v35, vcc, 0, v33, vcc
	global_load_dwordx2 v[164:165], v[34:35], off
	global_load_dwordx2 v[162:163], v[34:35], off offset:32
	global_load_dwordx2 v[160:161], v[34:35], off offset:64
	global_load_dwordx2 v[158:159], v[34:35], off offset:96
	v_add_co_u32_e32 v34, vcc, s22, v32
	s_mov_b32 s22, 0x3a060000
	s_nop 0
	v_addc_co_u32_e32 v35, vcc, 0, v33, vcc
	v_add_co_u32_e32 v32, vcc, s22, v32
	global_load_dwordx2 v[154:155], v[34:35], off
	global_load_dwordx2 v[150:151], v[34:35], off offset:32
	global_load_dwordx2 v[148:149], v[34:35], off offset:64
	global_load_dwordx2 v[146:147], v[34:35], off offset:96
	v_addc_co_u32_e32 v33, vcc, 0, v33, vcc
	global_load_dwordx2 v[142:143], v[32:33], off
	global_load_dwordx2 v[140:141], v[32:33], off offset:32
	global_load_dwordx2 v[138:139], v[32:33], off offset:64
	global_load_dwordx2 v[136:137], v[32:33], off offset:96
	ds_read_b128 v[32:35], v196
	ds_read_b128 v[40:43], v196 offset:4096
	ds_read_b128 v[56:59], v196 offset:8192
	ds_read_b128 v[72:75], v196 offset:12288
	ds_read_b128 v[60:63], v197
	ds_read_b128 v[64:67], v197 offset:4352
	ds_read_b128 v[68:71], v197 offset:8704
	ds_read_b128 v[80:83], v197 offset:13056
	s_waitcnt lgkmcnt(3)
	v_mfma_f32_16x16x32_bf16 v[108:111], v[60:63], v[32:35], 0
	s_movk_i32 s22, 0xc0
	v_lshl_add_u64 v[120:121], v[120:121], 0, s[62:63]
	v_lshl_add_u64 v[124:125], v[124:125], 0, s[60:61]
	s_waitcnt lgkmcnt(2)
	v_mfma_f32_16x16x32_bf16 v[104:107], v[64:67], v[32:35], 0
	v_lshl_add_u64 v[126:127], v[126:127], 0, s[60:61]
	v_lshl_add_u64 v[128:129], v[128:129], 0, s[62:63]
	v_lshl_add_u64 v[130:131], v[130:131], 0, s[62:63]
	s_waitcnt lgkmcnt(1)
	v_mfma_f32_16x16x32_bf16 v[96:99], v[68:71], v[32:35], 0
	v_lshl_add_u64 v[132:133], v[132:133], 0, s[62:63]
	s_waitcnt lgkmcnt(0)
	v_mfma_f32_16x16x32_bf16 v[88:91], v[80:83], v[32:35], 0
	v_mfma_f32_16x16x32_bf16 v[76:79], v[60:63], v[40:43], 0
	v_mfma_f32_16x16x32_bf16 v[32:35], v[64:67], v[40:43], 0
	v_mfma_f32_16x16x32_bf16 v[36:39], v[68:71], v[40:43], 0
	v_mfma_f32_16x16x32_bf16 v[40:43], v[80:83], v[40:43], 0
	v_mfma_f32_16x16x32_bf16 v[44:47], v[60:63], v[56:59], 0
	v_mfma_f32_16x16x32_bf16 v[48:51], v[64:67], v[56:59], 0
	v_mfma_f32_16x16x32_bf16 v[52:55], v[68:71], v[56:59], 0
	v_mfma_f32_16x16x32_bf16 v[56:59], v[80:83], v[56:59], 0
	v_mfma_f32_16x16x32_bf16 v[60:63], v[60:63], v[72:75], 0
	v_mfma_f32_16x16x32_bf16 v[64:67], v[64:67], v[72:75], 0
	v_mfma_f32_16x16x32_bf16 v[68:71], v[68:71], v[72:75], 0
	v_mfma_f32_16x16x32_bf16 v[72:75], v[80:83], v[72:75], 0
	ds_read_b128 v[100:103], v198
	ds_read_b128 v[92:95], v198 offset:4096
	ds_read_b128 v[84:87], v198 offset:8192
	ds_read_b128 v[80:83], v198 offset:12288
	ds_read_b128 v[202:205], v197 offset:64
	ds_read_b128 v[206:209], v197 offset:4416
	ds_read_b128 v[210:213], v197 offset:8768
	ds_read_b128 v[214:217], v197 offset:13120
	s_waitcnt lgkmcnt(3)
	v_mfma_f32_16x16x32_bf16 v[108:111], v[202:205], v[100:103], v[108:111]
	s_waitcnt lgkmcnt(2)
	v_mfma_f32_16x16x32_bf16 v[104:107], v[206:209], v[100:103], v[104:107]
	s_waitcnt lgkmcnt(1)
	v_mfma_f32_16x16x32_bf16 v[96:99], v[210:213], v[100:103], v[96:99]
	s_waitcnt lgkmcnt(0)
	v_mfma_f32_16x16x32_bf16 v[88:91], v[214:217], v[100:103], v[88:91]
	v_mfma_f32_16x16x32_bf16 v[76:79], v[202:205], v[92:95], v[76:79]
	v_mfma_f32_16x16x32_bf16 v[32:35], v[206:209], v[92:95], v[32:35]
	v_mfma_f32_16x16x32_bf16 v[36:39], v[210:213], v[92:95], v[36:39]
	v_mfma_f32_16x16x32_bf16 v[40:43], v[214:217], v[92:95], v[40:43]
	v_mfma_f32_16x16x32_bf16 v[44:47], v[202:205], v[84:87], v[44:47]
	v_mfma_f32_16x16x32_bf16 v[48:51], v[206:209], v[84:87], v[48:51]
	v_mfma_f32_16x16x32_bf16 v[52:55], v[210:213], v[84:87], v[52:55]
	v_mfma_f32_16x16x32_bf16 v[56:59], v[214:217], v[84:87], v[56:59]
	v_mfma_f32_16x16x32_bf16 v[60:63], v[202:205], v[80:83], v[60:63]
	v_mfma_f32_16x16x32_bf16 v[64:67], v[206:209], v[80:83], v[64:67]
	v_mfma_f32_16x16x32_bf16 v[68:71], v[210:213], v[80:83], v[68:71]
	v_mfma_f32_16x16x32_bf16 v[72:75], v[214:217], v[80:83], v[72:75]
	ds_read_b128 v[80:83], v199
	ds_read_b128 v[84:87], v199 offset:4096
	ds_read_b128 v[92:95], v199 offset:8192
	ds_read_b128 v[100:103], v199 offset:12288
	ds_read_b128 v[202:205], v197 offset:128
	ds_read_b128 v[206:209], v197 offset:4480
	ds_read_b128 v[210:213], v197 offset:8832
	ds_read_b128 v[214:217], v197 offset:13184
	s_waitcnt lgkmcnt(3)
	v_mfma_f32_16x16x32_bf16 v[108:111], v[202:205], v[80:83], v[108:111]
	s_waitcnt lgkmcnt(2)
	v_mfma_f32_16x16x32_bf16 v[104:107], v[206:209], v[80:83], v[104:107]
	s_waitcnt lgkmcnt(1)
	v_mfma_f32_16x16x32_bf16 v[96:99], v[210:213], v[80:83], v[96:99]
	s_waitcnt lgkmcnt(0)
; #define LAS __attribute__((address_space(3)))
; __device__ __forceinline__ void phase_sgu(CArgs a, LAS unsigned char* lds, int i2, int wv, int xw  ) {
;     ...
;             for (int ks = 0; ks < 4; ++ks) {
;                 bf16x8 bfr[4], af[4];
; #pragma unroll
;                 for (int m = 0; m < 4; ++m) { const int i = wr * 64 + m * 16 + fr; af[m] = *(const LAS bf16x8*)(wl + i * 256 + (((ks * 4 + fq) ^ (i & 15)) * 16)); }
; #pragma unroll
;                 for (int n = 0; n < 4; ++n) bfr[n] = *(const LAS bf16x8*)(vt + (wc * 64 + n * 16 + fr) * VS + ks * 32 + fq * 8);
; #pragma unroll
;                 for (int m = 0; m < 4; ++m)
; #pragma unroll
;                     for (int n = 0; n < 4; ++n) acc[m][n] = __builtin_amdgcn_mfma_f32_16x16x32_bf16(bfr[n], af[m], acc[m][n], 0, 0, 0);
;             }
;             { int te = tz; asm volatile("" : "+v"(te));
;               const int le = te & 63, we = te >> 6, wr = we >> 2, wc = we & 3, fr = le & 15, fq = le >> 4;
; #pragma unroll
;             for (int m = 0; m < 4; ++m) { const int i = wr * 64 + m * 16 + fr; const float bs = bsp[m];
; #pragma unroll
;                 for (int n = 0; n < 4; ++n) { const int cc = h * 256 + wc * 64 + n * 16 + 4 * fq;
;                     const f32x4 sv = acc[m][n] + bs; const u32x2 uv = uvp[m][n];
;                     *(unsigned*)(YQ + (tok0 + i) * SGU_W + cc) = pk4_fp8(bflo(uv.x) * sv.x * QS_GATED, bfhi(uv.x) * sv.y * QS_GATED, bflo(uv.y) * sv.z * QS_GATED, bfhi(uv.y) * sv.w * QS_GATED); } } }
	v_mfma_f32_16x16x32_bf16 v[80:83], v[214:217], v[80:83], v[88:91]
	v_mfma_f32_16x16x32_bf16 v[76:79], v[202:205], v[84:87], v[76:79]
	v_mfma_f32_16x16x32_bf16 v[32:35], v[206:209], v[84:87], v[32:35]
	v_mfma_f32_16x16x32_bf16 v[36:39], v[210:213], v[84:87], v[36:39]
	v_mfma_f32_16x16x32_bf16 v[40:43], v[214:217], v[84:87], v[40:43]
	v_mfma_f32_16x16x32_bf16 v[44:47], v[202:205], v[92:95], v[44:47]
	v_mfma_f32_16x16x32_bf16 v[48:51], v[206:209], v[92:95], v[48:51]
	v_mfma_f32_16x16x32_bf16 v[52:55], v[210:213], v[92:95], v[52:55]
	v_mfma_f32_16x16x32_bf16 v[84:87], v[214:217], v[92:95], v[56:59]
	v_mfma_f32_16x16x32_bf16 v[88:91], v[202:205], v[100:103], v[60:63]
	v_mfma_f32_16x16x32_bf16 v[92:95], v[206:209], v[100:103], v[64:67]
	v_mfma_f32_16x16x32_bf16 v[202:205], v[210:213], v[100:103], v[68:71]
	v_mfma_f32_16x16x32_bf16 v[100:103], v[214:217], v[100:103], v[72:75]
	ds_read_b128 v[56:59], v200
	ds_read_b128 v[60:63], v200 offset:4096
	ds_read_b128 v[206:209], v200 offset:8192
	ds_read_b128 v[210:213], v200 offset:12288
	ds_read_b128 v[214:217], v197 offset:192
	ds_read_b128 v[218:221], v197 offset:4544
	ds_read_b128 v[222:225], v197 offset:8896
	ds_read_b128 v[226:229], v197 offset:13248
	s_waitcnt lgkmcnt(3)
	v_mfma_f32_16x16x32_bf16 v[108:111], v[214:217], v[56:59], v[108:111]
	s_waitcnt lgkmcnt(2)
	v_mfma_f32_16x16x32_bf16 v[104:107], v[218:221], v[56:59], v[104:107]
	s_waitcnt lgkmcnt(1)
	v_mfma_f32_16x16x32_bf16 v[96:99], v[222:225], v[56:59], v[96:99]
	s_waitcnt lgkmcnt(0)
	v_mfma_f32_16x16x32_bf16 v[80:83], v[226:229], v[56:59], v[80:83]
	v_mfma_f32_16x16x32_bf16 v[56:59], v[218:221], v[206:209], v[48:51]
	v_mfma_f32_16x16x32_bf16 v[48:51], v[226:229], v[206:209], v[84:87]
	s_waitcnt vmcnt(19)
	s_nop 4
	v_pk_add_f32 v[80:81], v[168:169], v[80:81] op_sel_hi:[0,1]
	v_pk_add_f32 v[82:83], v[168:169], v[82:83] op_sel_hi:[0,1]
	s_waitcnt vmcnt(17)
	v_pk_add_f32 v[56:57], v[144:145], v[56:57] op_sel_hi:[0,1]
	v_mov_b32_e32 v85, v112
	v_bfe_u32 v248, v112, 4, 2
	v_mov_b32_e32 v249, 0
	v_mul_u32_u24_e32 v248, 12, v248
	v_mfma_f32_16x16x32_bf16 v[76:79], v[214:217], v[60:63], v[76:79]
	v_and_b32_e32 v84, 15, v85
	v_ashrrev_i32_e32 v86, 2, v85
	v_and_or_b32 v84, v86, s39, v84
	v_lshrrev_b32_e32 v86, 2, v85
	v_and_b32_e32 v86, 12, v86
	v_and_or_b32 v85, v85, s22, v86
	v_add_u32_e32 v152, s24, v85
	v_ashrrev_i32_e32 v85, 31, v84
	v_mfma_f32_16x16x32_bf16 v[72:75], v[218:221], v[60:63], v[32:35]
	v_lshl_add_u64 v[86:87], s[20:21], 0, v[84:85]
	s_waitcnt vmcnt(15)
	v_lshlrev_b32_e32 v85, 16, v174
	v_lshlrev_b64 v[86:87], 11, v[86:87]
	v_mfma_f32_16x16x32_bf16 v[68:71], v[222:225], v[60:63], v[36:39]
	v_lshl_add_u64 v[86:87], s[10:11], 0, v[86:87]
	v_lshl_add_u64 v[86:87], v[86:87], 0, v[152:153]
	v_pk_add_f32 v[76:77], v[156:157], v[76:77] op_sel_hi:[0,1]
	v_mfma_f32_16x16x32_bf16 v[64:67], v[226:229], v[60:63], v[40:43]
	v_add_f32_e64 v78, v156, v78
	v_add_f32_e64 v79, v156, v79
	v_pk_add_f32 v[72:73], v[156:157], v[72:73] op_sel_hi:[0,1]
	v_pk_add_f32 v[74:75], v[156:157], v[74:75] op_sel_hi:[0,1]
	v_mfma_f32_16x16x32_bf16 v[60:63], v[214:217], v[206:209], v[44:47]
	v_add_f32_e64 v68, v156, v68
	v_add_f32_e64 v69, v156, v69
	v_pk_add_f32 v[70:71], v[156:157], v[70:71] op_sel_hi:[0,1]
	v_pk_add_f32 v[64:65], v[156:157], v[64:65] op_sel_hi:[0,1]
	v_mfma_f32_16x16x32_bf16 v[44:47], v[214:217], v[210:213], v[88:91]
	v_add_f32_e64 v66, v156, v66
	v_add_f32_e64 v67, v156, v67
	s_nop 0
	v_pk_add_f32 v[60:61], v[144:145], v[60:61] op_sel_hi:[0,1]
	v_pk_add_f32 v[62:63], v[144:145], v[62:63] op_sel_hi:[0,1]
	v_pk_add_f32 v[90:91], v[168:169], v[108:109] op_sel_hi:[0,1]
	v_mul_f32_e32 v85, v90, v85
	v_and_b32_e32 v90, 0xffff0000, v174
	v_pk_add_f32 v[88:89], v[168:169], v[110:111] op_sel_hi:[0,1]
	v_mul_f32_e32 v90, v91, v90
	v_lshlrev_b32_e32 v91, 16, v175
	v_mul_f32_e32 v85, 0x41000000, v85
	v_mul_f32_e32 v90, 0x41000000, v90
	v_mul_f32_e32 v88, v88, v91
	v_and_b32_e32 v91, 0xffff0000, v175
	v_mul_f32_e32 v89, v89, v91
	v_med3_f32 v85, v85, s51, v187
	v_med3_f32 v90, v90, s51, v187
	v_cvt_pk_fp8_f32 v232, v85, v90
	v_mul_f32_e32 v88, 0x41000000, v88
	v_mul_f32_e32 v89, 0x41000000, v89
	v_med3_f32 v88, v88, s51, v187
	v_med3_f32 v89, v89, s51, v187
	v_cvt_pk_fp8_f32 v232, v88, v89 op_sel:[0,0,1]
	s_waitcnt vmcnt(14)
	v_lshlrev_b32_e32 v85, 16, v172
	v_pk_add_f32 v[88:89], v[168:169], v[106:107] op_sel_hi:[0,1]
	v_mfma_f32_16x16x32_bf16 v[52:55], v[222:225], v[206:209], v[52:55]
	v_pk_add_f32 v[90:91], v[168:169], v[104:105] op_sel_hi:[0,1]
	v_mul_f32_e32 v85, v90, v85
	v_and_b32_e32 v90, 0xffff0000, v172
	v_mul_f32_e32 v90, v91, v90
	v_lshlrev_b32_e32 v91, 16, v173
	v_mul_f32_e32 v85, 0x41000000, v85
	v_mul_f32_e32 v90, 0x41000000, v90
	v_mul_f32_e32 v88, v88, v91
	v_and_b32_e32 v91, 0xffff0000, v173
	v_mul_f32_e32 v89, v89, v91
	v_med3_f32 v85, v85, s51, v187
	v_med3_f32 v90, v90, s51, v187
	v_cvt_pk_fp8_f32 v233, v85, v90
	v_mul_f32_e32 v88, 0x41000000, v88
	v_mul_f32_e32 v89, 0x41000000, v89
	v_med3_f32 v88, v88, s51, v187
	v_med3_f32 v89, v89, s51, v187
	v_cvt_pk_fp8_f32 v233, v88, v89 op_sel:[0,0,1]
	s_waitcnt vmcnt(13)
	v_lshlrev_b32_e32 v85, 16, v170
	v_pk_add_f32 v[88:89], v[168:169], v[98:99] op_sel_hi:[0,1]
	v_pk_add_f32 v[58:59], v[144:145], v[58:59] op_sel_hi:[0,1]
	v_pk_add_f32 v[90:91], v[168:169], v[96:97] op_sel_hi:[0,1]
	v_mul_f32_e32 v85, v90, v85
	v_and_b32_e32 v90, 0xffff0000, v170
	v_mul_f32_e32 v90, v91, v90
	v_lshlrev_b32_e32 v91, 16, v171
	v_mul_f32_e32 v85, 0x41000000, v85
	v_mul_f32_e32 v90, 0x41000000, v90
	v_mul_f32_e32 v88, v88, v91
	v_and_b32_e32 v91, 0xffff0000, v171
	v_mul_f32_e32 v89, v89, v91
	v_med3_f32 v85, v85, s51, v187
	v_med3_f32 v90, v90, s51, v187
	v_cvt_pk_fp8_f32 v234, v85, v90
	s_waitcnt vmcnt(12)
; __device__ __forceinline__ void phase_sgu(CArgs a, LAS unsigned char* lds, int i2, int wv, int xw  ) {
;     ...
;             for (int m = 0; m < 4; ++m) { const int i = wr * 64 + m * 16 + fr; const float bs = bsp[m];
; #pragma unroll
;                 for (int n = 0; n < 4; ++n) { const int cc = h * 256 + wc * 64 + n * 16 + 4 * fq;
;                     const f32x4 sv = acc[m][n] + bs; const u32x2 uv = uvp[m][n];
;                     *(unsigned*)(YQ + (tok0 + i) * SGU_W + cc) = pk4_fp8(bflo(uv.x) * sv.x * QS_GATED, bfhi(uv.x) * sv.y * QS_GATED, bflo(uv.y) * sv.z * QS_GATED, bfhi(uv.y) * sv.w * QS_GATED); } } }
	v_lshlrev_b32_e32 v85, 16, v166
	v_mul_f32_e32 v80, v80, v85
	v_and_b32_e32 v85, 0xffff0000, v166
	v_mul_f32_e32 v81, v81, v85
	v_lshlrev_b32_e32 v85, 16, v167
	v_mul_f32_e32 v80, 0x41000000, v80
	v_mul_f32_e32 v81, 0x41000000, v81
	v_mul_f32_e32 v82, v82, v85
	v_and_b32_e32 v85, 0xffff0000, v167
	v_mul_f32_e32 v83, v83, v85
	v_med3_f32 v80, v80, s51, v187
	v_med3_f32 v81, v81, s51, v187
	v_cvt_pk_fp8_f32 v235, v80, v81
	v_mul_f32_e32 v82, 0x41000000, v82
	v_mul_f32_e32 v83, 0x41000000, v83
	v_med3_f32 v82, v82, s51, v187
	v_med3_f32 v83, v83, s51, v187
	v_cvt_pk_fp8_f32 v235, v82, v83 op_sel:[0,0,1]
	s_waitcnt vmcnt(11)
	v_lshlrev_b32_e32 v82, 16, v164
	v_mul_f32_e32 v76, v76, v82
	v_and_b32_e32 v82, 0xffff0000, v164
	v_mul_f32_e32 v77, v77, v82
	v_lshlrev_b32_e32 v82, 16, v165
	v_mul_f32_e32 v76, 0x41000000, v76
	v_mul_f32_e32 v77, 0x41000000, v77
	v_mul_f32_e32 v78, v78, v82
	v_and_b32_e32 v82, 0xffff0000, v165
	v_mul_f32_e32 v79, v79, v82
	v_med3_f32 v76, v76, s51, v187
	v_med3_f32 v77, v77, s51, v187
	v_cvt_pk_fp8_f32 v236, v76, v77
	v_mul_f32_e32 v78, 0x41000000, v78
	v_mul_f32_e32 v79, 0x41000000, v79
	v_med3_f32 v78, v78, s51, v187
	v_med3_f32 v79, v79, s51, v187
	v_cvt_pk_fp8_f32 v236, v78, v79 op_sel:[0,0,1]
	s_waitcnt vmcnt(10)
	v_lshlrev_b32_e32 v78, 16, v162
	v_mul_f32_e32 v72, v72, v78
	v_and_b32_e32 v78, 0xffff0000, v162
	v_mul_f32_e32 v73, v73, v78
	v_lshlrev_b32_e32 v78, 16, v163
	v_mul_f32_e32 v72, 0x41000000, v72
	v_mul_f32_e32 v73, 0x41000000, v73
	v_mul_f32_e32 v74, v74, v78
	v_and_b32_e32 v78, 0xffff0000, v163
	v_mul_f32_e32 v75, v75, v78
	v_med3_f32 v72, v72, s51, v187
	v_med3_f32 v73, v73, s51, v187
	v_cvt_pk_fp8_f32 v237, v72, v73
	s_waitcnt vmcnt(9)
	v_lshlrev_b32_e32 v72, 16, v160
	v_mul_f32_e32 v68, v68, v72
	v_and_b32_e32 v72, 0xffff0000, v160
	v_mul_f32_e32 v69, v69, v72
	v_lshlrev_b32_e32 v72, 16, v161
	v_mul_f32_e32 v68, 0x41000000, v68
	v_mul_f32_e32 v69, 0x41000000, v69
	v_mul_f32_e32 v70, v70, v72
	v_and_b32_e32 v72, 0xffff0000, v161
	v_mul_f32_e32 v71, v71, v72
	v_med3_f32 v68, v68, s51, v187
	v_med3_f32 v69, v69, s51, v187
	v_cvt_pk_fp8_f32 v238, v68, v69
	s_waitcnt vmcnt(8)
	v_lshlrev_b32_e32 v68, 16, v158
	v_mul_f32_e32 v64, v64, v68
	v_and_b32_e32 v68, 0xffff0000, v158
	v_mul_f32_e32 v65, v65, v68
	v_lshlrev_b32_e32 v68, 16, v159
	v_mul_f32_e32 v64, 0x41000000, v64
	v_mul_f32_e32 v65, 0x41000000, v65
	v_mul_f32_e32 v66, v66, v68
	v_and_b32_e32 v68, 0xffff0000, v159
	v_mul_f32_e32 v67, v67, v68
	v_med3_f32 v64, v64, s51, v187
	v_med3_f32 v65, v65, s51, v187
	v_cvt_pk_fp8_f32 v239, v64, v65
	v_mul_f32_e32 v66, 0x41000000, v66
	v_mul_f32_e32 v67, 0x41000000, v67
	v_med3_f32 v66, v66, s51, v187
	v_med3_f32 v67, v67, s51, v187
	v_cvt_pk_fp8_f32 v239, v66, v67 op_sel:[0,0,1]
	s_waitcnt vmcnt(7)
	v_lshlrev_b32_e32 v66, 16, v154
	v_mul_f32_e32 v60, v60, v66
	v_and_b32_e32 v66, 0xffff0000, v154
	v_mul_f32_e32 v61, v61, v66
	v_lshlrev_b32_e32 v66, 16, v155
	v_mul_f32_e32 v60, 0x41000000, v60
	v_mul_f32_e32 v61, 0x41000000, v61
	v_mul_f32_e32 v62, v62, v66
	v_and_b32_e32 v66, 0xffff0000, v155
	v_mul_f32_e32 v63, v63, v66
	v_med3_f32 v60, v60, s51, v187
	v_med3_f32 v61, v61, s51, v187
	v_cvt_pk_fp8_f32 v240, v60, v61
	v_mul_f32_e32 v62, 0x41000000, v62
	v_mul_f32_e32 v63, 0x41000000, v63
	v_med3_f32 v62, v62, s51, v187
	v_med3_f32 v63, v63, s51, v187
	v_cvt_pk_fp8_f32 v240, v62, v63 op_sel:[0,0,1]
	s_waitcnt vmcnt(6)
	v_lshlrev_b32_e32 v62, 16, v150
	v_mul_f32_e32 v56, v56, v62
	v_and_b32_e32 v62, 0xffff0000, v150
	v_mul_f32_e32 v57, v57, v62
	v_lshlrev_b32_e32 v62, 16, v151
	v_mul_f32_e32 v56, 0x41000000, v56
	v_mul_f32_e32 v57, 0x41000000, v57
	v_mul_f32_e32 v58, v58, v62
	v_and_b32_e32 v62, 0xffff0000, v151
	v_mul_f32_e32 v59, v59, v62
	v_med3_f32 v56, v56, s51, v187
	v_med3_f32 v57, v57, s51, v187
	v_cvt_pk_fp8_f32 v241, v56, v57
	v_pk_add_f32 v[52:53], v[144:145], v[52:53] op_sel_hi:[0,1]
	s_waitcnt vmcnt(5)
	v_lshlrev_b32_e32 v56, 16, v148
	v_mul_f32_e32 v52, v52, v56
	v_and_b32_e32 v56, 0xffff0000, v148
	v_pk_add_f32 v[54:55], v[144:145], v[54:55] op_sel_hi:[0,1]
	v_mul_f32_e32 v53, v53, v56
	v_lshlrev_b32_e32 v56, 16, v149
	v_mul_f32_e32 v52, 0x41000000, v52
	v_mul_f32_e32 v53, 0x41000000, v53
	v_mul_f32_e32 v54, v54, v56
	v_and_b32_e32 v56, 0xffff0000, v149
	v_mul_f32_e32 v55, v55, v56
	v_med3_f32 v52, v52, s51, v187
	v_med3_f32 v53, v53, s51, v187
	v_cvt_pk_fp8_f32 v242, v52, v53
	v_pk_add_f32 v[48:49], v[144:145], v[48:49] op_sel_hi:[0,1]
	s_waitcnt vmcnt(4)
	v_lshlrev_b32_e32 v52, 16, v146
	v_mul_f32_e32 v48, v48, v52
	v_and_b32_e32 v52, 0xffff0000, v146
	v_pk_add_f32 v[50:51], v[144:145], v[50:51] op_sel_hi:[0,1]
	v_mul_f32_e32 v49, v49, v52
	v_lshlrev_b32_e32 v52, 16, v147
	v_mul_f32_e32 v48, 0x41000000, v48
	v_mul_f32_e32 v49, 0x41000000, v49
	v_mul_f32_e32 v50, v50, v52
	v_and_b32_e32 v52, 0xffff0000, v147
	v_mul_f32_e32 v51, v51, v52
	v_med3_f32 v48, v48, s51, v187
	v_med3_f32 v49, v49, s51, v187
	v_cvt_pk_fp8_f32 v243, v48, v49
	v_mul_f32_e32 v50, 0x41000000, v50
	v_mul_f32_e32 v51, 0x41000000, v51
	v_med3_f32 v50, v50, s51, v187
	v_med3_f32 v51, v51, s51, v187
	v_cvt_pk_fp8_f32 v243, v50, v51 op_sel:[0,0,1]
	v_pk_add_f32 v[44:45], v[134:135], v[44:45] op_sel_hi:[0,1]
	s_waitcnt vmcnt(3)
; __device__ __forceinline__ void phase_sgu(CArgs a, LAS unsigned char* lds, int i2, int wv, int xw  ) {
;     ...
;             { int te = tz; asm volatile("" : "+v"(te));
;               const int le = te & 63, we = te >> 6, wr = we >> 2, wc = we & 3, fr = le & 15, fq = le >> 4;
; #pragma unroll
;             for (int m = 0; m < 4; ++m) { const int i = wr * 64 + m * 16 + fr; const float bs = bsp[m];
; #pragma unroll
;                 for (int n = 0; n < 4; ++n) { const int cc = h * 256 + wc * 64 + n * 16 + 4 * fq;
;                     const f32x4 sv = acc[m][n] + bs; const u32x2 uv = uvp[m][n];
;                     *(unsigned*)(YQ + (tok0 + i) * SGU_W + cc) = pk4_fp8(bflo(uv.x) * sv.x * QS_GATED, bfhi(uv.x) * sv.y * QS_GATED, bflo(uv.y) * sv.z * QS_GATED, bfhi(uv.y) * sv.w * QS_GATED); } } }
;             __syncthreads();
	v_lshlrev_b32_e32 v50, 16, v142
	v_mul_f32_e32 v44, v44, v50
	v_and_b32_e32 v50, 0xffff0000, v142
	v_pk_add_f32 v[46:47], v[134:135], v[46:47] op_sel_hi:[0,1]
	v_mul_f32_e32 v45, v45, v50
	v_lshlrev_b32_e32 v50, 16, v143
	v_mul_f32_e32 v44, 0x41000000, v44
	v_mul_f32_e32 v45, 0x41000000, v45
	v_mul_f32_e32 v46, v46, v50
	v_and_b32_e32 v50, 0xffff0000, v143
	v_mul_f32_e32 v47, v47, v50
	v_med3_f32 v44, v44, s51, v187
	v_med3_f32 v45, v45, s51, v187
	v_mfma_f32_16x16x32_bf16 v[40:43], v[218:221], v[210:213], v[92:95]
	v_cvt_pk_fp8_f32 v244, v44, v45
	v_mul_f32_e32 v46, 0x41000000, v46
	v_mul_f32_e32 v47, 0x41000000, v47
	v_med3_f32 v46, v46, s51, v187
	v_med3_f32 v47, v47, s51, v187
	v_cvt_pk_fp8_f32 v244, v46, v47 op_sel:[0,0,1]
	s_nop 1
	v_pk_add_f32 v[40:41], v[134:135], v[40:41] op_sel_hi:[0,1]
	s_waitcnt vmcnt(2)
	v_lshlrev_b32_e32 v46, 16, v140
	v_mfma_f32_16x16x32_bf16 v[36:39], v[222:225], v[210:213], v[202:205]
	v_mul_f32_e32 v40, v40, v46
	v_and_b32_e32 v46, 0xffff0000, v140
	v_pk_add_f32 v[42:43], v[134:135], v[42:43] op_sel_hi:[0,1]
	v_mul_f32_e32 v41, v41, v46
	v_lshlrev_b32_e32 v46, 16, v141
	v_mul_f32_e32 v40, 0x41000000, v40
	v_mul_f32_e32 v41, 0x41000000, v41
	v_mul_f32_e32 v42, v42, v46
	v_and_b32_e32 v46, 0xffff0000, v141
	v_mul_f32_e32 v43, v43, v46
	v_med3_f32 v40, v40, s51, v187
	v_med3_f32 v41, v41, s51, v187
	v_cvt_pk_fp8_f32 v245, v40, v41
	v_pk_add_f32 v[36:37], v[134:135], v[36:37] op_sel_hi:[0,1]
	s_waitcnt vmcnt(1)
	v_lshlrev_b32_e32 v40, 16, v138
	v_mfma_f32_16x16x32_bf16 v[32:35], v[226:229], v[210:213], v[100:103]
	v_mul_f32_e32 v36, v36, v40
	v_and_b32_e32 v40, 0xffff0000, v138
	v_pk_add_f32 v[38:39], v[134:135], v[38:39] op_sel_hi:[0,1]
	v_mul_f32_e32 v37, v37, v40
	v_lshlrev_b32_e32 v40, 16, v139
	v_mul_f32_e32 v36, 0x41000000, v36
	v_mul_f32_e32 v37, 0x41000000, v37
	v_mul_f32_e32 v38, v38, v40
	v_and_b32_e32 v40, 0xffff0000, v139
	v_mul_f32_e32 v39, v39, v40
	v_med3_f32 v36, v36, s51, v187
	v_med3_f32 v37, v37, s51, v187
	v_cvt_pk_fp8_f32 v246, v36, v37
	v_pk_add_f32 v[32:33], v[134:135], v[32:33] op_sel_hi:[0,1]
	s_waitcnt vmcnt(0)
	v_lshlrev_b32_e32 v36, 16, v136
	v_mul_f32_e32 v32, v32, v36
	v_and_b32_e32 v36, 0xffff0000, v136
	v_pk_add_f32 v[34:35], v[134:135], v[34:35] op_sel_hi:[0,1]
	v_mul_f32_e32 v33, v33, v36
	v_lshlrev_b32_e32 v36, 16, v137
	v_mul_f32_e32 v32, 0x41000000, v32
	v_mul_f32_e32 v33, 0x41000000, v33
	v_mul_f32_e32 v34, v34, v36
	v_and_b32_e32 v36, 0xffff0000, v137
	v_mul_f32_e32 v35, v35, v36
	v_med3_f32 v32, v32, s51, v187
	v_med3_f32 v33, v33, s51, v187
	v_cvt_pk_fp8_f32 v247, v32, v33
	v_mul_f32_e32 v88, 0x41000000, v88
	v_mul_f32_e32 v89, 0x41000000, v89
	v_or_b32_e32 v80, 16, v84
	v_mul_f32_e32 v74, 0x41000000, v74
	v_mul_f32_e32 v75, 0x41000000, v75
	v_mul_f32_e32 v70, 0x41000000, v70
	v_mul_f32_e32 v71, 0x41000000, v71
	v_or_b32_e32 v64, 32, v84
	v_mul_f32_e32 v58, 0x41000000, v58
	v_mul_f32_e32 v59, 0x41000000, v59
	v_mul_f32_e32 v54, 0x41000000, v54
	v_mul_f32_e32 v55, 0x41000000, v55
	v_or_b32_e32 v48, 48, v84
	v_mul_f32_e32 v42, 0x41000000, v42
	v_mul_f32_e32 v43, 0x41000000, v43
	v_mul_f32_e32 v38, 0x41000000, v38
	v_mul_f32_e32 v39, 0x41000000, v39
	v_mul_f32_e32 v34, 0x41000000, v34
	v_mul_f32_e32 v35, 0x41000000, v35
	v_med3_f32 v88, v88, s51, v187
	v_med3_f32 v89, v89, s51, v187
	v_ashrrev_i32_e32 v81, 31, v80
	v_med3_f32 v74, v74, s51, v187
	v_med3_f32 v75, v75, s51, v187
	v_med3_f32 v70, v70, s51, v187
	v_med3_f32 v71, v71, s51, v187
	v_ashrrev_i32_e32 v65, 31, v64
	v_med3_f32 v58, v58, s51, v187
	v_med3_f32 v59, v59, s51, v187
	v_med3_f32 v54, v54, s51, v187
	v_med3_f32 v55, v55, s51, v187
	v_ashrrev_i32_e32 v49, 31, v48
	v_med3_f32 v42, v42, s51, v187
	v_med3_f32 v43, v43, s51, v187
	v_med3_f32 v38, v38, s51, v187
	v_med3_f32 v39, v39, s51, v187
	v_med3_f32 v34, v34, s51, v187
	v_med3_f32 v35, v35, s51, v187
	v_cvt_pk_fp8_f32 v234, v88, v89 op_sel:[0,0,1]
	v_lshl_add_u64 v[80:81], s[20:21], 0, v[80:81]
	v_cvt_pk_fp8_f32 v237, v74, v75 op_sel:[0,0,1]
	v_cvt_pk_fp8_f32 v238, v70, v71 op_sel:[0,0,1]
	v_lshl_add_u64 v[64:65], s[20:21], 0, v[64:65]
	v_cvt_pk_fp8_f32 v241, v58, v59 op_sel:[0,0,1]
	v_cvt_pk_fp8_f32 v242, v54, v55 op_sel:[0,0,1]
	v_lshl_add_u64 v[48:49], s[20:21], 0, v[48:49]
	v_cvt_pk_fp8_f32 v245, v42, v43 op_sel:[0,0,1]
	v_cvt_pk_fp8_f32 v246, v38, v39 op_sel:[0,0,1]
	v_cvt_pk_fp8_f32 v247, v34, v35 op_sel:[0,0,1]
	v_lshlrev_b64 v[80:81], 11, v[80:81]
	v_lshlrev_b64 v[64:65], 11, v[64:65]
	v_lshlrev_b64 v[48:49], 11, v[48:49]
	v_lshl_add_u64 v[80:81], s[10:11], 0, v[80:81]
	v_lshl_add_u64 v[64:65], s[10:11], 0, v[64:65]
	v_lshl_add_u64 v[48:49], s[10:11], 0, v[48:49]
	s_addk_i32 s24, 0x100
	v_lshl_add_u64 v[76:77], v[80:81], 0, v[152:153]
	v_lshl_add_u64 v[60:61], v[64:65], 0, v[152:153]
	v_lshl_add_u64 v[44:45], v[48:49], 0, v[152:153]
	s_cmpk_eq_i32 s6, 0x1000
	v_permlane16_swap_b32_e32 v232, v233
	v_permlane16_swap_b32_e32 v234, v235
	v_permlane16_swap_b32_e32 v236, v237
	v_permlane16_swap_b32_e32 v238, v239
	v_permlane16_swap_b32_e32 v240, v241
	v_permlane16_swap_b32_e32 v242, v243
	v_permlane16_swap_b32_e32 v244, v245
	v_permlane16_swap_b32_e32 v246, v247
	v_lshl_add_u64 v[178:179], v[86:87], 0, v[248:249]
	v_lshl_add_u64 v[180:181], v[76:77], 0, v[248:249]
	v_lshl_add_u64 v[230:231], v[60:61], 0, v[248:249]
	v_lshl_add_u64 v[250:251], v[44:45], 0, v[248:249]
	v_permlane32_swap_b32_e32 v232, v234
	v_permlane32_swap_b32_e32 v233, v235
	v_permlane32_swap_b32_e32 v236, v238
	v_permlane32_swap_b32_e32 v237, v239
	v_permlane32_swap_b32_e32 v240, v242
	v_permlane32_swap_b32_e32 v241, v243
	v_permlane32_swap_b32_e32 v244, v246
	v_permlane32_swap_b32_e32 v245, v247
	s_nop 1
	global_store_dwordx4 v[178:179], v[232:235], off
	global_store_dwordx4 v[180:181], v[236:239], off
	global_store_dwordx4 v[230:231], v[240:243], off
	global_store_dwordx4 v[250:251], v[244:247], off
	s_barrier
	s_cbranch_scc1 .LBB0_279
; #define LAS __attribute__((address_space(3)))
; __device__ __forceinline__ unsigned pk2(float lo, float hi) { unsigned r; asm("v_cvt_pk_bf16_f32 %0, %1, %2" : "=v"(r) : "v"(lo), "v"(hi)); return r; }
; __device__ __forceinline__ void phase_sgu(CArgs a, LAS unsigned char* lds, int i2, int wv, int xw  ) {
;     ...
;         for (int hh = 0; hh < 4; ++hh) {
;             const int h = h0 + hh;
;             const bf16* wm = (const bf16*)(a->ws + WS_WSGU) + ((size_t)i2 * 8 + h) * 128 * 128;
; #pragma unroll
;             for (int q = 0; q < 4; ++q) { const int r = 4 * (8 * q + wave) + (lane >> 4);
;                 __builtin_amdgcn_global_load_lds((const unsigned*)(wm + (size_t)r * 128 + 8 * ((lane & 15) ^ (r & 15))), (LAS unsigned*)(wl + (8 * q + wave) * 1024), 16, 0, 0); }
;             {
;                 const int cA = 2 * wave + (lane >> 5);
;                 f32x4 gg[2][2], bb[2][2];
; #pragma unroll
;                 for (int q = 0; q < 2; ++q) { const float* gp = lg + h * 256 + (cA + 16 * q) * 8; const float* bp = lb + h * 256 + (cA + 16 * q) * 8;
;                     gg[q][0] = *(const f32x4*)gp; gg[q][1] = *(const f32x4*)(gp + 4); bb[q][0] = *(const f32x4*)bp; bb[q][1] = *(const f32x4*)(bp + 4); }
; #pragma unroll
;                 for (int it = 0; it < 8; ++it) { const int j = 32 * (it & 3) + (lane & 31), q = it >> 2, c8 = cA + 16 * q;
;                     const float m = mu[j], r = rs[j]; const u32x4 raw = vraw[it];
;                     const float v[8] = {bflo(raw.x), bfhi(raw.x), bflo(raw.y), bfhi(raw.y), bflo(raw.z), bfhi(raw.z), bflo(raw.w), bfhi(raw.w)};
; #pragma unroll
;                     for (int k = 0; k < 8; k += 2) { const unsigned pr = pk2((v[k] - m) * r * gg[q][k >> 2][k & 3] + bb[q][k >> 2][k & 3], (v[k + 1] - m) * r * gg[q][k >> 2][(k + 1) & 3] + bb[q][k >> 2][(k + 1) & 3]);
;                         vt[(c8 * 8 + k) * VS + j] = (bf16)(pr & 0xffffu); vt[(c8 * 8 + k + 1) * VS + j] = (bf16)(pr >> 16); } }
.LBB0_284:
	s_add_i32 s22, 0, 0x12000
	v_lshl_add_u64 v[32:33], s[4:5], 0, v[116:117]
	s_add_i32 m0, s22, s25
	v_lshl_add_u64 v[36:37], v[118:119], 0, s[6:7]
	global_load_lds_dwordx4 v[32:33], off
	v_lshl_add_u64 v[32:33], s[4:5], 0, v[122:123]
	s_add_i32 m0, s22, s28
	v_lshl_add_u64 v[44:45], v[114:115], 0, s[6:7]
	global_load_lds_dwordx4 v[32:33], off
	v_lshl_add_u64 v[32:33], s[4:5], 0, v[124:125]
	s_add_i32 m0, s22, s33
	v_lshlrev_b32_e32 v66, 16, v0
	global_load_lds_dwordx4 v[32:33], off
	v_lshl_add_u64 v[32:33], s[4:5], 0, v[126:127]
	s_add_i32 m0, s22, s40
	v_and_b32_e32 v67, 0xffff0000, v0
	global_load_lds_dwordx4 v[32:33], off
	global_load_dwordx4 v[48:51], v[36:37], off offset:16
	global_load_dwordx4 v[56:59], v[36:37], off
	global_load_dwordx4 v[52:55], v[44:45], off offset:16
	global_load_dwordx4 v[60:63], v[44:45], off
	s_nop 0
	global_load_dwordx4 v[32:35], v[36:37], off offset:528
	global_load_dwordx4 v[40:43], v[36:37], off offset:512
	s_nop 0
	global_load_dwordx4 v[36:39], v[44:45], off offset:528
	s_nop 0
	global_load_dwordx4 v[44:47], v[44:45], off offset:512
	ds_read_b32 v64, v113
	ds_read_b32 v65, v145
	v_lshlrev_b32_e32 v68, 16, v1
	v_and_b32_e32 v69, 0xffff0000, v1
	v_lshlrev_b32_e32 v70, 16, v2
	s_waitcnt lgkmcnt(0)
	v_sub_f32_e32 v66, v66, v64
	v_mul_f32_e32 v66, v65, v66
	v_sub_f32_e32 v67, v67, v64
	v_mul_f32_e32 v67, v65, v67
	v_and_b32_e32 v71, 0xffff0000, v2
	v_lshlrev_b32_e32 v72, 16, v3
	v_and_b32_e32 v73, 0xffff0000, v3
	v_lshlrev_b32_e32 v74, 16, v7
	v_and_b32_e32 v75, 0xffff0000, v7
	v_lshlrev_b32_e32 v76, 16, v11
	v_and_b32_e32 v77, 0xffff0000, v11
	v_lshlrev_b32_e32 v78, 16, v15
	v_and_b32_e32 v79, 0xffff0000, v15
	s_cmpk_eq_i32 s6, 0xc00
	s_waitcnt vmcnt(0)
	v_fma_f32 v66, v56, v66, v60
	v_fma_f32 v67, v57, v67, v61
	v_cvt_pk_bf16_f32 v66, v66, v67
	ds_write_b16 v157, v66
	ds_write_b16_d16_hi v157, v66 offset:272
	v_sub_f32_e32 v66, v68, v64
	v_mul_f32_e32 v66, v65, v66
	v_sub_f32_e32 v67, v69, v64
	v_fma_f32 v66, v58, v66, v62
	v_mul_f32_e32 v67, v65, v67
	v_fma_f32 v67, v59, v67, v63
	v_cvt_pk_bf16_f32 v66, v66, v67
	ds_write_b16 v157, v66 offset:544
	ds_write_b16_d16_hi v157, v66 offset:816
	v_sub_f32_e32 v66, v70, v64
	v_mul_f32_e32 v66, v65, v66
	v_sub_f32_e32 v67, v71, v64
	v_fma_f32 v66, v48, v66, v52
	v_mul_f32_e32 v67, v65, v67
	v_fma_f32 v67, v49, v67, v53
	v_cvt_pk_bf16_f32 v66, v66, v67
	ds_write_b16 v157, v66 offset:1088
	ds_write_b16_d16_hi v157, v66 offset:1360
	v_sub_f32_e32 v66, v72, v64
	v_mul_f32_e32 v66, v65, v66
	v_sub_f32_e32 v67, v73, v64
	v_fma_f32 v66, v50, v66, v54
	v_mul_f32_e32 v67, v65, v67
	v_fma_f32 v67, v51, v67, v55
	v_cvt_pk_bf16_f32 v66, v66, v67
	ds_write_b16 v157, v66 offset:1632
	ds_write_b16_d16_hi v157, v66 offset:1904
	ds_read_b32 v66, v169
	ds_read_b32 v67, v176
	v_lshlrev_b32_e32 v68, 16, v4
	v_and_b32_e32 v69, 0xffff0000, v4
	v_lshlrev_b32_e32 v70, 16, v5
	s_waitcnt lgkmcnt(1)
	v_sub_f32_e32 v68, v68, v66
	s_waitcnt lgkmcnt(0)
	v_mul_f32_e32 v68, v67, v68
	v_sub_f32_e32 v69, v69, v66
	v_fma_f32 v68, v56, v68, v60
	v_mul_f32_e32 v69, v67, v69
	v_fma_f32 v69, v57, v69, v61
	v_cvt_pk_bf16_f32 v68, v68, v69
	v_and_b32_e32 v71, 0xffff0000, v5
	ds_write_b16 v157, v68 offset:64
	ds_write_b16_d16_hi v157, v68 offset:336
	v_sub_f32_e32 v68, v70, v66
	v_mul_f32_e32 v68, v67, v68
	v_sub_f32_e32 v69, v71, v66
	v_fma_f32 v68, v58, v68, v62
	v_mul_f32_e32 v69, v67, v69
	v_lshlrev_b32_e32 v72, 16, v6
	v_fma_f32 v69, v59, v69, v63
	v_cvt_pk_bf16_f32 v68, v68, v69
	v_and_b32_e32 v73, 0xffff0000, v6
	ds_write_b16 v157, v68 offset:608
	ds_write_b16_d16_hi v157, v68 offset:880
	v_sub_f32_e32 v68, v72, v66
	v_mul_f32_e32 v68, v67, v68
	v_sub_f32_e32 v69, v73, v66
	v_fma_f32 v68, v48, v68, v52
	v_mul_f32_e32 v69, v67, v69
	v_fma_f32 v69, v49, v69, v53
	v_cvt_pk_bf16_f32 v68, v68, v69
	ds_write_b16 v157, v68 offset:1152
	ds_write_b16_d16_hi v157, v68 offset:1424
	v_sub_f32_e32 v68, v74, v66
	v_mul_f32_e32 v68, v67, v68
	v_sub_f32_e32 v69, v75, v66
	v_fma_f32 v68, v50, v68, v54
	v_mul_f32_e32 v69, v67, v69
	v_fma_f32 v69, v51, v69, v55
	v_cvt_pk_bf16_f32 v68, v68, v69
	ds_write_b16 v157, v68 offset:1696
	ds_write_b16_d16_hi v157, v68 offset:1968
	ds_read_b32 v68, v177
	ds_read_b32 v69, v192
	v_lshlrev_b32_e32 v70, 16, v8
	v_and_b32_e32 v71, 0xffff0000, v8
	v_lshlrev_b32_e32 v72, 16, v9
	s_waitcnt lgkmcnt(1)
	v_sub_f32_e32 v70, v70, v68
	s_waitcnt lgkmcnt(0)
	v_mul_f32_e32 v70, v69, v70
	v_sub_f32_e32 v71, v71, v68
	v_fma_f32 v70, v56, v70, v60
	v_mul_f32_e32 v71, v69, v71
	v_fma_f32 v71, v57, v71, v61
	v_cvt_pk_bf16_f32 v70, v70, v71
	v_and_b32_e32 v73, 0xffff0000, v9
	ds_write_b16 v157, v70 offset:128
	ds_write_b16_d16_hi v157, v70 offset:400
	v_sub_f32_e32 v70, v72, v68
	v_mul_f32_e32 v70, v69, v70
	v_sub_f32_e32 v71, v73, v68
	v_fma_f32 v70, v58, v70, v62
	v_mul_f32_e32 v71, v69, v71
	v_lshlrev_b32_e32 v74, 16, v10
	v_fma_f32 v71, v59, v71, v63
	v_cvt_pk_bf16_f32 v70, v70, v71
	v_and_b32_e32 v75, 0xffff0000, v10
	ds_write_b16 v157, v70 offset:672
	ds_write_b16_d16_hi v157, v70 offset:944
	v_sub_f32_e32 v70, v74, v68
	v_mul_f32_e32 v70, v69, v70
	v_sub_f32_e32 v71, v75, v68
	v_fma_f32 v70, v48, v70, v52
	v_mul_f32_e32 v71, v69, v71
	v_fma_f32 v71, v49, v71, v53
	v_cvt_pk_bf16_f32 v70, v70, v71
	ds_write_b16 v157, v70 offset:1216
	ds_write_b16_d16_hi v157, v70 offset:1488
	v_sub_f32_e32 v70, v76, v68
	v_mul_f32_e32 v70, v69, v70
	v_sub_f32_e32 v71, v77, v68
	v_fma_f32 v70, v50, v70, v54
	v_mul_f32_e32 v71, v69, v71
	v_fma_f32 v71, v51, v71, v55
	v_cvt_pk_bf16_f32 v70, v70, v71
	ds_write_b16 v157, v70 offset:1760
	ds_write_b16_d16_hi v157, v70 offset:2032
	ds_read_b32 v70, v193
	ds_read_b32 v71, v194
	v_lshlrev_b32_e32 v72, 16, v12
	v_and_b32_e32 v73, 0xffff0000, v12
	v_lshlrev_b32_e32 v74, 16, v13
	s_waitcnt lgkmcnt(1)
; __device__ __forceinline__ unsigned pk2(float lo, float hi) { unsigned r; asm("v_cvt_pk_bf16_f32 %0, %1, %2" : "=v"(r) : "v"(lo), "v"(hi)); return r; }
; __device__ __forceinline__ void phase_sgu(CArgs a, LAS unsigned char* lds, int i2, int wv, int xw  ) {
;     ...
;                 for (int it = 0; it < 8; ++it) { const int j = 32 * (it & 3) + (lane & 31), q = it >> 2, c8 = cA + 16 * q;
;                     const float m = mu[j], r = rs[j]; const u32x4 raw = vraw[it];
;                     const float v[8] = {bflo(raw.x), bfhi(raw.x), bflo(raw.y), bfhi(raw.y), bflo(raw.z), bfhi(raw.z), bflo(raw.w), bfhi(raw.w)};
; #pragma unroll
;                     for (int k = 0; k < 8; k += 2) { const unsigned pr = pk2((v[k] - m) * r * gg[q][k >> 2][k & 3] + bb[q][k >> 2][k & 3], (v[k + 1] - m) * r * gg[q][k >> 2][(k + 1) & 3] + bb[q][k >> 2][(k + 1) & 3]);
;                         vt[(c8 * 8 + k) * VS + j] = (bf16)(pr & 0xffffu); vt[(c8 * 8 + k + 1) * VS + j] = (bf16)(pr >> 16); } }
	v_sub_f32_e32 v72, v72, v70
	s_waitcnt lgkmcnt(0)
	v_mul_f32_e32 v72, v71, v72
	v_fma_f32 v56, v56, v72, v60
	v_sub_f32_e32 v60, v73, v70
	v_mul_f32_e32 v60, v71, v60
	v_fma_f32 v57, v57, v60, v61
	v_cvt_pk_bf16_f32 v56, v56, v57
	v_and_b32_e32 v75, 0xffff0000, v13
	ds_write_b16 v157, v56 offset:192
	ds_write_b16_d16_hi v157, v56 offset:464
	v_sub_f32_e32 v56, v74, v70
	v_mul_f32_e32 v56, v71, v56
	v_sub_f32_e32 v57, v75, v70
	v_fma_f32 v56, v58, v56, v62
	v_mul_f32_e32 v57, v71, v57
	v_lshlrev_b32_e32 v76, 16, v14
	v_fmac_f32_e32 v63, v59, v57
	v_cvt_pk_bf16_f32 v56, v56, v63
	ds_write_b16 v157, v56 offset:736
	ds_write_b16_d16_hi v157, v56 offset:1008
	v_sub_f32_e32 v56, v76, v70
	v_and_b32_e32 v77, 0xffff0000, v14
	v_mul_f32_e32 v56, v71, v56
	v_fma_f32 v48, v48, v56, v52
	v_sub_f32_e32 v52, v77, v70
	v_mul_f32_e32 v52, v71, v52
	v_fma_f32 v49, v49, v52, v53
	v_cvt_pk_bf16_f32 v48, v48, v49
	ds_write_b16 v157, v48 offset:1280
	ds_write_b16_d16_hi v157, v48 offset:1552
	v_sub_f32_e32 v48, v78, v70
	v_mul_f32_e32 v48, v71, v48
	v_sub_f32_e32 v49, v79, v70
	v_fma_f32 v48, v50, v48, v54
	v_mul_f32_e32 v49, v71, v49
	v_fmac_f32_e32 v55, v51, v49
	v_cvt_pk_bf16_f32 v48, v48, v55
	ds_write_b16 v157, v48 offset:1824
	ds_write_b16_d16_hi v157, v48 offset:2096
	v_lshlrev_b32_e32 v48, 16, v16
	v_and_b32_e32 v49, 0xffff0000, v16
	v_sub_f32_e32 v48, v48, v64
	v_mul_f32_e32 v48, v65, v48
	v_sub_f32_e32 v49, v49, v64
	v_fma_f32 v48, v40, v48, v44
	v_mul_f32_e32 v49, v65, v49
	v_lshlrev_b32_e32 v50, 16, v17
	v_fma_f32 v49, v41, v49, v45
	v_cvt_pk_bf16_f32 v48, v48, v49
	v_and_b32_e32 v51, 0xffff0000, v17
	ds_write_b16 v195, v48
	ds_write_b16_d16_hi v195, v48 offset:272
	v_sub_f32_e32 v48, v50, v64
	v_mul_f32_e32 v48, v65, v48
	v_sub_f32_e32 v49, v51, v64
	v_fma_f32 v48, v42, v48, v46
	v_mul_f32_e32 v49, v65, v49
	v_lshlrev_b32_e32 v52, 16, v18
	v_fma_f32 v49, v43, v49, v47
	v_cvt_pk_bf16_f32 v48, v48, v49
	v_and_b32_e32 v53, 0xffff0000, v18
	ds_write_b16 v157, v48 offset:35360
	ds_write_b16_d16_hi v157, v48 offset:35632
	v_sub_f32_e32 v48, v52, v64
	v_mul_f32_e32 v48, v65, v48
	v_sub_f32_e32 v49, v53, v64
	v_fma_f32 v48, v32, v48, v36
	v_mul_f32_e32 v49, v65, v49
	v_lshlrev_b32_e32 v54, 16, v19
	v_fma_f32 v49, v33, v49, v37
	v_cvt_pk_bf16_f32 v48, v48, v49
	v_and_b32_e32 v55, 0xffff0000, v19
	ds_write_b16 v157, v48 offset:35904
	ds_write_b16_d16_hi v157, v48 offset:36176
	v_sub_f32_e32 v48, v54, v64
	v_mul_f32_e32 v48, v65, v48
	v_sub_f32_e32 v49, v55, v64
	v_fma_f32 v48, v34, v48, v38
	v_mul_f32_e32 v49, v65, v49
	v_fma_f32 v49, v35, v49, v39
	v_cvt_pk_bf16_f32 v48, v48, v49
	ds_write_b16 v157, v48 offset:36448
	ds_write_b16_d16_hi v157, v48 offset:36720
	v_lshlrev_b32_e32 v48, 16, v20
	v_and_b32_e32 v49, 0xffff0000, v20
	v_sub_f32_e32 v48, v48, v66
	v_mul_f32_e32 v48, v67, v48
	v_sub_f32_e32 v49, v49, v66
	v_fma_f32 v48, v40, v48, v44
	v_mul_f32_e32 v49, v67, v49
	v_lshlrev_b32_e32 v50, 16, v21
	v_fma_f32 v49, v41, v49, v45
	v_cvt_pk_bf16_f32 v48, v48, v49
	v_and_b32_e32 v51, 0xffff0000, v21
	ds_write_b16 v195, v48 offset:64
	ds_write_b16_d16_hi v195, v48 offset:336
	v_sub_f32_e32 v48, v50, v66
	v_mul_f32_e32 v48, v67, v48
	v_sub_f32_e32 v49, v51, v66
	v_fma_f32 v48, v42, v48, v46
	v_mul_f32_e32 v49, v67, v49
	v_lshlrev_b32_e32 v52, 16, v22
	v_fma_f32 v49, v43, v49, v47
	v_cvt_pk_bf16_f32 v48, v48, v49
	v_and_b32_e32 v53, 0xffff0000, v22
	ds_write_b16 v157, v48 offset:35424
	ds_write_b16_d16_hi v157, v48 offset:35696
	v_sub_f32_e32 v48, v52, v66
	v_mul_f32_e32 v48, v67, v48
	v_sub_f32_e32 v49, v53, v66
	v_fma_f32 v48, v32, v48, v36
	v_mul_f32_e32 v49, v67, v49
	v_lshlrev_b32_e32 v54, 16, v23
	v_fma_f32 v49, v33, v49, v37
	v_cvt_pk_bf16_f32 v48, v48, v49
	v_and_b32_e32 v55, 0xffff0000, v23
	ds_write_b16 v157, v48 offset:35968
	ds_write_b16_d16_hi v157, v48 offset:36240
	v_sub_f32_e32 v48, v54, v66
	v_mul_f32_e32 v48, v67, v48
	v_sub_f32_e32 v49, v55, v66
	v_fma_f32 v48, v34, v48, v38
	v_mul_f32_e32 v49, v67, v49
	v_fma_f32 v49, v35, v49, v39
	v_cvt_pk_bf16_f32 v48, v48, v49
	ds_write_b16 v157, v48 offset:36512
	ds_write_b16_d16_hi v157, v48 offset:36784
	v_lshlrev_b32_e32 v48, 16, v24
	v_and_b32_e32 v49, 0xffff0000, v24
	v_sub_f32_e32 v48, v48, v68
	v_mul_f32_e32 v48, v69, v48
	v_sub_f32_e32 v49, v49, v68
	v_fma_f32 v48, v40, v48, v44
	v_mul_f32_e32 v49, v69, v49
	v_lshlrev_b32_e32 v50, 16, v25
	v_fma_f32 v49, v41, v49, v45
	v_cvt_pk_bf16_f32 v48, v48, v49
	v_and_b32_e32 v51, 0xffff0000, v25
	ds_write_b16 v195, v48 offset:128
	ds_write_b16_d16_hi v195, v48 offset:400
	v_sub_f32_e32 v48, v50, v68
	v_mul_f32_e32 v48, v69, v48
	v_sub_f32_e32 v49, v51, v68
	v_fma_f32 v48, v42, v48, v46
	v_mul_f32_e32 v49, v69, v49
	v_lshlrev_b32_e32 v52, 16, v26
	v_fma_f32 v49, v43, v49, v47
	v_cvt_pk_bf16_f32 v48, v48, v49
	v_and_b32_e32 v53, 0xffff0000, v26
	ds_write_b16 v157, v48 offset:35488
	ds_write_b16_d16_hi v157, v48 offset:35760
	v_sub_f32_e32 v48, v52, v68
	v_mul_f32_e32 v48, v69, v48
	v_sub_f32_e32 v49, v53, v68
	v_fma_f32 v48, v32, v48, v36
	v_mul_f32_e32 v49, v69, v49
	v_lshlrev_b32_e32 v54, 16, v27
	v_fma_f32 v49, v33, v49, v37
	v_cvt_pk_bf16_f32 v48, v48, v49
	v_and_b32_e32 v55, 0xffff0000, v27
	ds_write_b16 v157, v48 offset:36032
	ds_write_b16_d16_hi v157, v48 offset:36304
	v_sub_f32_e32 v48, v54, v68
	v_mul_f32_e32 v48, v69, v48
	v_sub_f32_e32 v49, v55, v68
	v_fma_f32 v48, v34, v48, v38
	v_mul_f32_e32 v49, v69, v49
	v_fma_f32 v49, v35, v49, v39
	v_cvt_pk_bf16_f32 v48, v48, v49
	ds_write_b16 v157, v48 offset:36576
	ds_write_b16_d16_hi v157, v48 offset:36848
	v_lshlrev_b32_e32 v48, 16, v28
	v_sub_f32_e32 v48, v48, v70
	v_and_b32_e32 v49, 0xffff0000, v28
	v_mul_f32_e32 v48, v71, v48
	v_fma_f32 v40, v40, v48, v44
	v_sub_f32_e32 v44, v49, v70
	v_mul_f32_e32 v44, v71, v44
	v_lshlrev_b32_e32 v50, 16, v29
	v_fma_f32 v41, v41, v44, v45
	v_cvt_pk_bf16_f32 v40, v40, v41
	v_and_b32_e32 v51, 0xffff0000, v29
	ds_write_b16 v195, v40 offset:192
	ds_write_b16_d16_hi v195, v40 offset:464
	v_sub_f32_e32 v40, v50, v70
	v_mul_f32_e32 v40, v71, v40
	v_sub_f32_e32 v41, v51, v70
	v_fma_f32 v40, v42, v40, v46
	v_mul_f32_e32 v41, v71, v41
	v_lshlrev_b32_e32 v52, 16, v30
	v_fmac_f32_e32 v47, v43, v41
	v_cvt_pk_bf16_f32 v40, v40, v47
	ds_write_b16 v157, v40 offset:35552
	ds_write_b16_d16_hi v157, v40 offset:35824
	v_sub_f32_e32 v40, v52, v70
	v_and_b32_e32 v53, 0xffff0000, v30
	v_mul_f32_e32 v40, v71, v40
	v_fma_f32 v32, v32, v40, v36
	v_sub_f32_e32 v36, v53, v70
	v_mul_f32_e32 v36, v71, v36
	v_lshlrev_b32_e32 v54, 16, v31
	v_fma_f32 v33, v33, v36, v37
	v_cvt_pk_bf16_f32 v32, v32, v33
	v_and_b32_e32 v55, 0xffff0000, v31
	ds_write_b16 v157, v32 offset:36096
	ds_write_b16_d16_hi v157, v32 offset:36368
	v_sub_f32_e32 v32, v54, v70
	v_mul_f32_e32 v32, v71, v32
	v_sub_f32_e32 v33, v55, v70
	v_fma_f32 v32, v34, v32, v38
	v_mul_f32_e32 v33, v71, v33
	v_fmac_f32_e32 v39, v35, v33
	v_cvt_pk_bf16_f32 v32, v32, v39
	ds_write_b16 v157, v32 offset:36640
	ds_write_b16_d16_hi v157, v32 offset:36912
	s_cbranch_scc1 .LBB0_283
; __device__ __forceinline__ void phase_sgu(CArgs a, LAS unsigned char* lds, int i2, int wv, int xw  ) {
;     ...
;             if (hh < 3) {
; #pragma unroll
;                 for (int it = 0; it < 8; ++it) { const int j = 32 * (it & 3) + (lane & 31), c8 = 2 * (8 * (it >> 2) + wave) + (lane >> 5);
;                     vraw[it] = *(const u32x4*)(HB + (tok0 + j) * (2 * SGU_W) + SGU_W + (h + 1) * 256 + c8 * 8); } }
;             asm volatile("s_waitcnt vmcnt(0)" ::: "memory");
;             __syncthreads();
	v_lshl_add_u64 v[8:9], s[4:5], 0, v[130:131]
	v_add_co_u32_e32 v0, vcc, 0x3a001000, v8
	v_lshl_add_u64 v[24:25], s[4:5], 0, v[128:129]
	s_nop 0
	v_addc_co_u32_e32 v1, vcc, 0, v9, vcc
	v_add_co_u32_e32 v4, vcc, 0x3a041000, v8
	s_mov_b32 s22, 0x3a001000
	s_nop 0
	v_addc_co_u32_e32 v5, vcc, 0, v9, vcc
	v_add_co_u32_e32 v10, vcc, 0x3a081000, v8
	global_load_dwordx4 v[0:3], v[0:1], off offset:512
	s_nop 0
	global_load_dwordx4 v[4:7], v[4:5], off offset:512
	v_addc_co_u32_e32 v11, vcc, 0, v9, vcc
	v_add_co_u32_e32 v12, vcc, 0x3a0c1000, v8
	s_nop 1
	v_addc_co_u32_e32 v13, vcc, 0, v9, vcc
	v_add_co_u32_e32 v16, vcc, s22, v24
	global_load_dwordx4 v[8:11], v[10:11], off offset:512
	s_nop 0
	global_load_dwordx4 v[12:15], v[12:13], off offset:512
	v_addc_co_u32_e32 v17, vcc, 0, v25, vcc
	v_add_co_u32_e32 v20, vcc, 0x3a041000, v24
	s_nop 1
	v_addc_co_u32_e32 v21, vcc, 0, v25, vcc
	v_add_co_u32_e32 v26, vcc, 0x3a081000, v24
	global_load_dwordx4 v[16:19], v[16:17], off offset:512
	s_nop 0
	global_load_dwordx4 v[20:23], v[20:21], off offset:512
	v_addc_co_u32_e32 v27, vcc, 0, v25, vcc
	v_add_co_u32_e32 v28, vcc, 0x3a0c1000, v24
	s_nop 1
	v_addc_co_u32_e32 v29, vcc, 0, v25, vcc
	global_load_dwordx4 v[24:27], v[26:27], off offset:512
	s_nop 0
	global_load_dwordx4 v[28:31], v[28:29], off offset:512
	s_waitcnt vmcnt(8)
	s_branch .Lo2_rows_inflight
